# v16 + gather (gate/up) GEMM K-loops: phase-1 MFMAs moved back between the phase-1 barriers (hipcc had sunk them into phase 2's read segment)
# speedup vs baseline: 1.0056x; 1.0029x over previous
.LBB0_1944:
	s_add_u32 s40, s36, 0x80
	s_addc_u32 s41, s37, 0
	v_add_u32_e32 v178, s5, v188
	s_and_b64 s[38:39], s[38:39], exec
	ds_read_b128 v[196:199], v178
	ds_read_b128 v[200:203], v178 offset:1024
	ds_read_b128 v[204:207], v178 offset:2048
	ds_read_b128 v[208:211], v178 offset:3072
	v_mov_b32_e32 v178, v181
	s_mov_b32 m0, s43
	s_cselect_b32 s39, s27, s23
	s_cselect_b32 s38, s26, s8
	s_waitcnt lgkmcnt(0)
	global_load_lds_dwordx4 v178, s[38:39]
	v_mov_b32_e32 v178, v183
	s_mov_b32 m0, s44
	s_cselect_b32 s41, s11, s41
	global_load_lds_dwordx4 v178, s[38:39]
	s_barrier
	s_waitcnt lgkmcnt(0)
	s_cselect_b32 s40, s10, s40
	s_setprio 1
	v_mfma_scale_f32_16x16x128_f8f6f4 v[160:163], v[196:203], v[40:47], v[160:163], v195, v195 op_sel_hi:[0,0,0]
	v_mfma_scale_f32_16x16x128_f8f6f4 v[152:155], v[204:211], v[40:47], v[152:155], v195, v195 op_sel_hi:[0,0,0]
	v_mfma_scale_f32_16x16x128_f8f6f4 v[148:151], v[196:203], v[32:39], v[148:151], v195, v195 op_sel_hi:[0,0,0]
	v_mfma_scale_f32_16x16x128_f8f6f4 v[144:147], v[204:211], v[32:39], v[144:147], v195, v195 op_sel_hi:[0,0,0]
	v_mfma_scale_f32_16x16x128_f8f6f4 v[136:139], v[196:203], v[24:31], v[136:139], v195, v195 op_sel_hi:[0,0,0]
	v_mfma_scale_f32_16x16x128_f8f6f4 v[128:131], v[204:211], v[24:31], v[128:131], v195, v195 op_sel_hi:[0,0,0]
	v_mfma_scale_f32_16x16x128_f8f6f4 v[124:127], v[196:203], v[16:23], v[124:127], v195, v195 op_sel_hi:[0,0,0]
	v_mfma_scale_f32_16x16x128_f8f6f4 v[116:119], v[204:211], v[16:23], v[116:119], v195, v195 op_sel_hi:[0,0,0]
	s_setprio 0
	v_mov_b32_e32 v178, v184
	s_mov_b32 m0, s31
	s_barrier
	ds_read_b128 v[16:19], v194 offset:16384
	ds_read_b128 v[20:23], v194 offset:17408
	ds_read_b128 v[24:27], v194 offset:18432
	ds_read_b128 v[28:31], v194 offset:19456
	ds_read_b128 v[32:35], v194 offset:20480
	ds_read_b128 v[36:39], v194 offset:21504
	ds_read_b128 v[40:43], v194 offset:22528
	ds_read_b128 v[44:47], v194 offset:23552
	s_nop 0
	global_load_lds_dwordx4 v178, s[40:41]
	v_mov_b32_e32 v178, v185
	s_mov_b32 m0, s45
	s_nop 0
	global_load_lds_dwordx4 v178, s[40:41]
	s_barrier
	s_waitcnt lgkmcnt(0)
	s_setprio 1
	s_waitcnt lgkmcnt(0)
	v_mfma_scale_f32_16x16x128_f8f6f4 v[108:111], v[0:7], v[16:23], v[108:111], v195, v195 op_sel_hi:[0,0,0]
	v_mfma_scale_f32_16x16x128_f8f6f4 v[100:103], v[8:15], v[16:23], v[100:103], v195, v195 op_sel_hi:[0,0,0]
	v_mfma_scale_f32_16x16x128_f8f6f4 v[92:95], v[0:7], v[24:31], v[92:95], v195, v195 op_sel_hi:[0,0,0]
	v_mfma_scale_f32_16x16x128_f8f6f4 v[84:87], v[8:15], v[24:31], v[84:87], v195, v195 op_sel_hi:[0,0,0]
	v_mfma_scale_f32_16x16x128_f8f6f4 v[76:79], v[0:7], v[32:39], v[76:79], v195, v195 op_sel_hi:[0,0,0]
	v_mfma_scale_f32_16x16x128_f8f6f4 v[68:71], v[8:15], v[32:39], v[68:71], v195, v195 op_sel_hi:[0,0,0]
	v_mfma_scale_f32_16x16x128_f8f6f4 v[60:63], v[0:7], v[40:47], v[60:63], v195, v195 op_sel_hi:[0,0,0]
	v_mfma_scale_f32_16x16x128_f8f6f4 v[52:55], v[8:15], v[40:47], v[52:55], v195, v195 op_sel_hi:[0,0,0]
	s_setprio 0
	s_barrier
	s_add_u32 s62, s38, 0x40000
	s_addc_u32 s63, s39, 0
	v_mov_b32_e32 v0, v181
	s_add_i32 s61, s5, s42
	s_mov_b32 m0, s61
	s_nop 0
	global_load_lds_dwordx4 v0, s[62:63]
	v_mov_b32_e32 v0, v183
	s_add_i32 m0, s61, 0x2000
	s_nop 0
	global_load_lds_dwordx4 v0, s[62:63]
	s_waitcnt vmcnt(6)
	s_barrier
	s_setprio 1
	v_mfma_scale_f32_16x16x128_f8f6f4 v[104:107], v[196:203], v[16:23], v[104:107], v195, v195 op_sel_hi:[0,0,0]
	v_mfma_scale_f32_16x16x128_f8f6f4 v[96:99], v[204:211], v[16:23], v[96:99], v195, v195 op_sel_hi:[0,0,0]
	v_mfma_scale_f32_16x16x128_f8f6f4 v[88:91], v[196:203], v[24:31], v[88:91], v195, v195 op_sel_hi:[0,0,0]
	v_mfma_scale_f32_16x16x128_f8f6f4 v[80:83], v[204:211], v[24:31], v[80:83], v195, v195 op_sel_hi:[0,0,0]
	v_mfma_scale_f32_16x16x128_f8f6f4 v[72:75], v[196:203], v[32:39], v[72:75], v195, v195 op_sel_hi:[0,0,0]
	v_mfma_scale_f32_16x16x128_f8f6f4 v[64:67], v[204:211], v[32:39], v[64:67], v195, v195 op_sel_hi:[0,0,0]
	v_mfma_scale_f32_16x16x128_f8f6f4 v[56:59], v[196:203], v[40:47], v[56:59], v195, v195 op_sel_hi:[0,0,0]
	v_mfma_scale_f32_16x16x128_f8f6f4 v[48:51], v[204:211], v[40:47], v[48:51], v195, v195 op_sel_hi:[0,0,0]
	s_setprio 0
	s_add_i32 s61, 0, 0x18000
	v_add_u32_e32 v12, s61, v188
	s_barrier
	ds_read_b128 v[0:3], v12
	ds_read_b128 v[4:7], v12 offset:1024
	ds_read_b128 v[8:11], v12 offset:2048
	ds_read_b128 v[12:15], v12 offset:3072
	v_mov_b32_e32 v178, v186
	s_mov_b32 m0, s46
	ds_read_b128 v[16:19], v194 offset:32768
	ds_read_b128 v[20:23], v194 offset:33792
	ds_read_b128 v[24:27], v194 offset:34816
	ds_read_b128 v[28:31], v194 offset:35840
	ds_read_b128 v[32:35], v194 offset:36864
	ds_read_b128 v[36:39], v194 offset:37888
	ds_read_b128 v[40:43], v194 offset:38912
	ds_read_b128 v[44:47], v194 offset:39936
	s_nop 0
	global_load_lds_dwordx4 v178, s[40:41]
	v_mov_b32_e32 v178, v187
	s_mov_b32 m0, s47
	s_nop 0
	global_load_lds_dwordx4 v178, s[40:41]
	s_waitcnt lgkmcnt(8)
	s_barrier
	s_waitcnt lgkmcnt(0)
	s_setprio 1
	s_waitcnt lgkmcnt(0)
	v_mfma_scale_f32_16x16x128_f8f6f4 v[172:175], v[0:7], v[16:23], v[172:175], v195, v195 op_sel_hi:[0,0,0]
	v_mfma_scale_f32_16x16x128_f8f6f4 v[168:171], v[8:15], v[16:23], v[168:171], v195, v195 op_sel_hi:[0,0,0]
	v_mfma_scale_f32_16x16x128_f8f6f4 v[164:167], v[0:7], v[24:31], v[164:167], v195, v195 op_sel_hi:[0,0,0]
	v_mfma_scale_f32_16x16x128_f8f6f4 v[156:159], v[8:15], v[24:31], v[156:159], v195, v195 op_sel_hi:[0,0,0]
	v_mfma_scale_f32_16x16x128_f8f6f4 v[140:143], v[0:7], v[32:39], v[140:143], v195, v195 op_sel_hi:[0,0,0]
	v_mfma_scale_f32_16x16x128_f8f6f4 v[132:135], v[8:15], v[32:39], v[132:135], v195, v195 op_sel_hi:[0,0,0]
	v_mfma_scale_f32_16x16x128_f8f6f4 v[120:123], v[0:7], v[40:47], v[120:123], v195, v195 op_sel_hi:[0,0,0]
	v_mfma_scale_f32_16x16x128_f8f6f4 v[112:115], v[8:15], v[40:47], v[112:115], v195, v195 op_sel_hi:[0,0,0]
	s_setprio 0
	s_barrier
	s_add_i32 s62, 0, 0x1c000
	v_add_u32_e32 v178, s62, v188
	ds_read_b128 v[196:199], v178
	ds_read_b128 v[200:203], v178 offset:1024
	ds_read_b128 v[204:207], v178 offset:2048
	ds_read_b128 v[208:211], v178 offset:3072
	v_mov_b32_e32 v178, v181
	s_add_i32 s61, s61, s42
	v_lshl_add_u64 v[212:213], s[38:39], 0, v[178:179]
	v_lshl_add_u64 v[212:213], v[212:213], 0, s[12:13]
	s_mov_b32 m0, s61
	v_mov_b32_e32 v178, v183
	global_load_lds_dwordx4 v[212:213], off
	s_add_i32 m0, s61, 0x2000
	v_lshl_add_u64 v[212:213], s[38:39], 0, v[178:179]
	v_lshl_add_u64 v[212:213], v[212:213], 0, s[12:13]
	global_load_lds_dwordx4 v[212:213], off
	s_barrier
	s_waitcnt lgkmcnt(0)
	s_setprio 1
	s_waitcnt lgkmcnt(0)
	v_mfma_scale_f32_16x16x128_f8f6f4 v[160:163], v[196:203], v[16:23], v[160:163], v195, v195 op_sel_hi:[0,0,0]
	v_mfma_scale_f32_16x16x128_f8f6f4 v[152:155], v[204:211], v[16:23], v[152:155], v195, v195 op_sel_hi:[0,0,0]
	v_mfma_scale_f32_16x16x128_f8f6f4 v[148:151], v[196:203], v[24:31], v[148:151], v195, v195 op_sel_hi:[0,0,0]
	v_mfma_scale_f32_16x16x128_f8f6f4 v[144:147], v[204:211], v[24:31], v[144:147], v195, v195 op_sel_hi:[0,0,0]
	v_mfma_scale_f32_16x16x128_f8f6f4 v[136:139], v[196:203], v[32:39], v[136:139], v195, v195 op_sel_hi:[0,0,0]
	v_mfma_scale_f32_16x16x128_f8f6f4 v[128:131], v[204:211], v[32:39], v[128:131], v195, v195 op_sel_hi:[0,0,0]
	v_mfma_scale_f32_16x16x128_f8f6f4 v[124:127], v[196:203], v[40:47], v[124:127], v195, v195 op_sel_hi:[0,0,0]
	v_mfma_scale_f32_16x16x128_f8f6f4 v[116:119], v[204:211], v[40:47], v[116:119], v195, v195 op_sel_hi:[0,0,0]
	s_setprio 0
	v_mov_b32_e32 v178, v184
	s_barrier
	ds_read_b128 v[16:19], v194 offset:49152
	ds_read_b128 v[20:23], v194 offset:50176
	ds_read_b128 v[24:27], v194 offset:51200
	ds_read_b128 v[28:31], v194 offset:52224
	ds_read_b128 v[32:35], v194 offset:53248
	ds_read_b128 v[36:39], v194 offset:54272
	ds_read_b128 v[40:43], v194 offset:55296
	ds_read_b128 v[44:47], v194 offset:56320
	s_mov_b32 m0, s52
	v_lshl_add_u64 v[212:213], s[40:41], 0, v[178:179]
	v_lshl_add_u64 v[212:213], v[212:213], 0, s[12:13]
	v_mov_b32_e32 v178, v185
	global_load_lds_dwordx4 v[212:213], off
	s_mov_b32 m0, s53
	v_lshl_add_u64 v[212:213], s[40:41], 0, v[178:179]
	v_lshl_add_u64 v[212:213], v[212:213], 0, s[12:13]
	global_load_lds_dwordx4 v[212:213], off
	s_barrier
	s_waitcnt lgkmcnt(0)
	s_setprio 1
	s_waitcnt lgkmcnt(0)
	v_mfma_scale_f32_16x16x128_f8f6f4 v[108:111], v[0:7], v[16:23], v[108:111], v195, v195 op_sel_hi:[0,0,0]
	v_mfma_scale_f32_16x16x128_f8f6f4 v[100:103], v[8:15], v[16:23], v[100:103], v195, v195 op_sel_hi:[0,0,0]
	v_mfma_scale_f32_16x16x128_f8f6f4 v[92:95], v[0:7], v[24:31], v[92:95], v195, v195 op_sel_hi:[0,0,0]
	v_mfma_scale_f32_16x16x128_f8f6f4 v[84:87], v[8:15], v[24:31], v[84:87], v195, v195 op_sel_hi:[0,0,0]
	v_mfma_scale_f32_16x16x128_f8f6f4 v[76:79], v[0:7], v[32:39], v[76:79], v195, v195 op_sel_hi:[0,0,0]
	v_mfma_scale_f32_16x16x128_f8f6f4 v[68:71], v[8:15], v[32:39], v[68:71], v195, v195 op_sel_hi:[0,0,0]
	v_mfma_scale_f32_16x16x128_f8f6f4 v[60:63], v[0:7], v[40:47], v[60:63], v195, v195 op_sel_hi:[0,0,0]
	v_mfma_scale_f32_16x16x128_f8f6f4 v[52:55], v[8:15], v[40:47], v[52:55], v195, v195 op_sel_hi:[0,0,0]
	s_setprio 0
	s_barrier
	s_add_u32 s38, s38, 0x40080
	s_addc_u32 s39, s39, 0
	v_mov_b32_e32 v0, v181
	s_add_i32 s40, s62, s42
	s_mov_b32 m0, s40
	s_nop 0
	global_load_lds_dwordx4 v0, s[38:39]
	v_mov_b32_e32 v0, v183
	s_add_i32 m0, s40, 0x2000
	s_nop 0
	global_load_lds_dwordx4 v0, s[38:39]
	s_waitcnt vmcnt(6)
	s_barrier
	s_setprio 1
	v_mfma_scale_f32_16x16x128_f8f6f4 v[104:107], v[196:203], v[16:23], v[104:107], v195, v195 op_sel_hi:[0,0,0]
	v_mfma_scale_f32_16x16x128_f8f6f4 v[96:99], v[204:211], v[16:23], v[96:99], v195, v195 op_sel_hi:[0,0,0]
	v_mfma_scale_f32_16x16x128_f8f6f4 v[88:91], v[196:203], v[24:31], v[88:91], v195, v195 op_sel_hi:[0,0,0]
	v_mfma_scale_f32_16x16x128_f8f6f4 v[80:83], v[204:211], v[24:31], v[80:83], v195, v195 op_sel_hi:[0,0,0]
	v_mfma_scale_f32_16x16x128_f8f6f4 v[72:75], v[196:203], v[32:39], v[72:75], v195, v195 op_sel_hi:[0,0,0]
	v_mfma_scale_f32_16x16x128_f8f6f4 v[64:67], v[204:211], v[32:39], v[64:67], v195, v195 op_sel_hi:[0,0,0]
	v_mfma_scale_f32_16x16x128_f8f6f4 v[56:59], v[196:203], v[40:47], v[56:59], v195, v195 op_sel_hi:[0,0,0]
	v_mfma_scale_f32_16x16x128_f8f6f4 v[48:51], v[204:211], v[40:47], v[48:51], v195, v195 op_sel_hi:[0,0,0]
	s_setprio 0
	s_add_i32 s60, s60, 2
	s_add_u32 s36, s36, 0x100
	s_addc_u32 s37, s37, 0
	s_add_u32 s8, s8, 0x100
	s_addc_u32 s23, s23, 0
	s_cmp_gt_u32 s60, 13
	s_barrier
	s_cbranch_scc1 .LBB0_1936
.LBB0_1945:
	ds_read_b128 v[0:3], v193
	ds_read_b128 v[4:7], v193 offset:1024
	ds_read_b128 v[8:11], v193 offset:2048
	ds_read_b128 v[12:15], v193 offset:3072
	s_cmp_eq_u32 s60, 12
	s_cselect_b64 s[38:39], -1, 0
	v_mov_b32_e32 v178, v186
	ds_read_b128 v[40:43], v194
	ds_read_b128 v[44:47], v194 offset:1024
	ds_read_b128 v[32:35], v194 offset:2048
	ds_read_b128 v[36:39], v194 offset:3072
	ds_read_b128 v[24:27], v194 offset:4096
	ds_read_b128 v[28:31], v194 offset:5120
	ds_read_b128 v[16:19], v194 offset:6144
	ds_read_b128 v[20:23], v194 offset:7168
	s_add_i32 m0, s31, 0xc000
	s_nop 0
	global_load_lds_dwordx4 v178, s[36:37]
	v_mov_b32_e32 v178, v187
	s_add_i32 m0, s31, 0xe000
	s_nop 0
	global_load_lds_dwordx4 v178, s[36:37]
	s_waitcnt lgkmcnt(8)
	s_barrier
	s_waitcnt lgkmcnt(0)
	s_setprio 1
	v_mfma_scale_f32_16x16x128_f8f6f4 v[172:175], v[0:7], v[40:47], v[172:175], v195, v195 op_sel_hi:[0,0,0]
	v_mfma_scale_f32_16x16x128_f8f6f4 v[168:171], v[8:15], v[40:47], v[168:171], v195, v195 op_sel_hi:[0,0,0]
	v_mfma_scale_f32_16x16x128_f8f6f4 v[164:167], v[0:7], v[32:39], v[164:167], v195, v195 op_sel_hi:[0,0,0]
	v_mfma_scale_f32_16x16x128_f8f6f4 v[156:159], v[8:15], v[32:39], v[156:159], v195, v195 op_sel_hi:[0,0,0]
	v_mfma_scale_f32_16x16x128_f8f6f4 v[140:143], v[0:7], v[24:31], v[140:143], v195, v195 op_sel_hi:[0,0,0]
	v_mfma_scale_f32_16x16x128_f8f6f4 v[132:135], v[8:15], v[24:31], v[132:135], v195, v195 op_sel_hi:[0,0,0]
	v_mfma_scale_f32_16x16x128_f8f6f4 v[120:123], v[0:7], v[16:23], v[120:123], v195, v195 op_sel_hi:[0,0,0]
	v_mfma_scale_f32_16x16x128_f8f6f4 v[112:115], v[8:15], v[16:23], v[112:115], v195, v195 op_sel_hi:[0,0,0]
	s_setprio 0
	s_barrier
	s_and_b64 s[40:41], s[34:35], s[38:39]
	s_andn2_b64 vcc, exec, s[40:41]
	s_cbranch_vccnz .LBB0_1944
	ds_read_b32 v178, v189
	ds_read_b32 v185, v190
	ds_read_b32 v186, v191
	ds_read_b32 v187, v192
	s_waitcnt lgkmcnt(0)
	v_lshl_add_u32 v184, v178, 11, v180
	v_lshl_add_u32 v185, v185, 11, v182
	v_lshl_add_u32 v186, v186, 11, v180
	v_lshl_add_u32 v187, v187, 11, v182
	s_branch .LBB0_1944
.Lpeelg_h0:
	ds_read_b128 v[0:3], v193
	ds_read_b128 v[4:7], v193 offset:1024
	ds_read_b128 v[8:11], v193 offset:2048
	ds_read_b128 v[12:15], v193 offset:3072
	s_cmp_eq_u32 s60, 12
	s_cselect_b64 s[38:39], -1, 0
	v_mov_b32_e32 v178, v186
	ds_read_b128 v[40:43], v194
	ds_read_b128 v[44:47], v194 offset:1024
	ds_read_b128 v[32:35], v194 offset:2048
	ds_read_b128 v[36:39], v194 offset:3072
	ds_read_b128 v[24:27], v194 offset:4096
	ds_read_b128 v[28:31], v194 offset:5120
	ds_read_b128 v[16:19], v194 offset:6144
	ds_read_b128 v[20:23], v194 offset:7168
	s_add_i32 m0, s31, 0xc000
	s_nop 0
	global_load_lds_dwordx4 v178, s[36:37]
	v_mov_b32_e32 v178, v187
	s_add_i32 m0, s31, 0xe000
	s_nop 0
	global_load_lds_dwordx4 v178, s[36:37]
	s_waitcnt lgkmcnt(8)
	s_barrier
	s_waitcnt lgkmcnt(0)
	s_setprio 1
	v_mfma_scale_f32_16x16x128_f8f6f4 v[172:175], v[0:7], v[40:47], 0, v195, v195 op_sel_hi:[0,0,0]
	v_mfma_scale_f32_16x16x128_f8f6f4 v[168:171], v[8:15], v[40:47], 0, v195, v195 op_sel_hi:[0,0,0]
	v_mfma_scale_f32_16x16x128_f8f6f4 v[164:167], v[0:7], v[32:39], 0, v195, v195 op_sel_hi:[0,0,0]
	v_mfma_scale_f32_16x16x128_f8f6f4 v[156:159], v[8:15], v[32:39], 0, v195, v195 op_sel_hi:[0,0,0]
	v_mfma_scale_f32_16x16x128_f8f6f4 v[140:143], v[0:7], v[24:31], 0, v195, v195 op_sel_hi:[0,0,0]
	v_mfma_scale_f32_16x16x128_f8f6f4 v[132:135], v[8:15], v[24:31], 0, v195, v195 op_sel_hi:[0,0,0]
	v_mfma_scale_f32_16x16x128_f8f6f4 v[120:123], v[0:7], v[16:23], 0, v195, v195 op_sel_hi:[0,0,0]
	v_mfma_scale_f32_16x16x128_f8f6f4 v[112:115], v[8:15], v[16:23], 0, v195, v195 op_sel_hi:[0,0,0]
	s_setprio 0
	s_barrier
	s_and_b64 s[40:41], s[34:35], s[38:39]
	s_andn2_b64 vcc, exec, s[40:41]
	s_cbranch_vccnz .Lpeelg_t0
	ds_read_b32 v178, v189
	ds_read_b32 v185, v190
	ds_read_b32 v186, v191
	ds_read_b32 v187, v192
	s_waitcnt lgkmcnt(0)
	v_lshl_add_u32 v184, v178, 11, v180
	v_lshl_add_u32 v185, v185, 11, v182
	v_lshl_add_u32 v186, v186, 11, v180
	v_lshl_add_u32 v187, v187, 11, v182
	s_branch .Lpeelg_t0
.Lpeelg_t0:
	s_add_u32 s40, s36, 0x80
	s_addc_u32 s41, s37, 0
	v_add_u32_e32 v178, s5, v188
	s_and_b64 s[38:39], s[38:39], exec
	ds_read_b128 v[196:199], v178
	ds_read_b128 v[200:203], v178 offset:1024
	ds_read_b128 v[204:207], v178 offset:2048
	ds_read_b128 v[208:211], v178 offset:3072
	v_mov_b32_e32 v178, v181
	s_mov_b32 m0, s43
	s_cselect_b32 s39, s27, s23
	s_cselect_b32 s38, s26, s8
	s_waitcnt lgkmcnt(0)
	global_load_lds_dwordx4 v178, s[38:39]
	v_mov_b32_e32 v178, v183
	s_mov_b32 m0, s44
	s_cselect_b32 s41, s11, s41
	global_load_lds_dwordx4 v178, s[38:39]
	s_barrier
	s_waitcnt lgkmcnt(0)
	s_cselect_b32 s40, s10, s40
	s_setprio 1
	v_mfma_scale_f32_16x16x128_f8f6f4 v[160:163], v[196:203], v[40:47], 0, v195, v195 op_sel_hi:[0,0,0]
	v_mfma_scale_f32_16x16x128_f8f6f4 v[152:155], v[204:211], v[40:47], 0, v195, v195 op_sel_hi:[0,0,0]
	v_mfma_scale_f32_16x16x128_f8f6f4 v[148:151], v[196:203], v[32:39], 0, v195, v195 op_sel_hi:[0,0,0]
	v_mfma_scale_f32_16x16x128_f8f6f4 v[144:147], v[204:211], v[32:39], 0, v195, v195 op_sel_hi:[0,0,0]
	v_mfma_scale_f32_16x16x128_f8f6f4 v[136:139], v[196:203], v[24:31], 0, v195, v195 op_sel_hi:[0,0,0]
	v_mfma_scale_f32_16x16x128_f8f6f4 v[128:131], v[204:211], v[24:31], 0, v195, v195 op_sel_hi:[0,0,0]
	v_mfma_scale_f32_16x16x128_f8f6f4 v[124:127], v[196:203], v[16:23], 0, v195, v195 op_sel_hi:[0,0,0]
	v_mfma_scale_f32_16x16x128_f8f6f4 v[116:119], v[204:211], v[16:23], 0, v195, v195 op_sel_hi:[0,0,0]
	s_setprio 0
	v_mov_b32_e32 v178, v184
	s_mov_b32 m0, s31
	s_barrier
	ds_read_b128 v[16:19], v194 offset:16384
	ds_read_b128 v[20:23], v194 offset:17408
	ds_read_b128 v[24:27], v194 offset:18432
	ds_read_b128 v[28:31], v194 offset:19456
	ds_read_b128 v[32:35], v194 offset:20480
	ds_read_b128 v[36:39], v194 offset:21504
	ds_read_b128 v[40:43], v194 offset:22528
	ds_read_b128 v[44:47], v194 offset:23552
	s_nop 0
	global_load_lds_dwordx4 v178, s[40:41]
	v_mov_b32_e32 v178, v185
	s_mov_b32 m0, s45
	s_nop 0
	global_load_lds_dwordx4 v178, s[40:41]
	s_barrier
	s_waitcnt lgkmcnt(0)
	s_setprio 1
	s_waitcnt lgkmcnt(0)
	v_mfma_scale_f32_16x16x128_f8f6f4 v[108:111], v[0:7], v[16:23], 0, v195, v195 op_sel_hi:[0,0,0]
	v_mfma_scale_f32_16x16x128_f8f6f4 v[100:103], v[8:15], v[16:23], 0, v195, v195 op_sel_hi:[0,0,0]
	v_mfma_scale_f32_16x16x128_f8f6f4 v[92:95], v[0:7], v[24:31], 0, v195, v195 op_sel_hi:[0,0,0]
	v_mfma_scale_f32_16x16x128_f8f6f4 v[84:87], v[8:15], v[24:31], 0, v195, v195 op_sel_hi:[0,0,0]
	v_mfma_scale_f32_16x16x128_f8f6f4 v[76:79], v[0:7], v[32:39], 0, v195, v195 op_sel_hi:[0,0,0]
	v_mfma_scale_f32_16x16x128_f8f6f4 v[68:71], v[8:15], v[32:39], 0, v195, v195 op_sel_hi:[0,0,0]
	v_mfma_scale_f32_16x16x128_f8f6f4 v[60:63], v[0:7], v[40:47], 0, v195, v195 op_sel_hi:[0,0,0]
	v_mfma_scale_f32_16x16x128_f8f6f4 v[52:55], v[8:15], v[40:47], 0, v195, v195 op_sel_hi:[0,0,0]
	s_setprio 0
	s_barrier
	s_add_u32 s62, s38, 0x40000
	s_addc_u32 s63, s39, 0
	v_mov_b32_e32 v0, v181
	s_add_i32 s61, s5, s42
	s_mov_b32 m0, s61
	s_nop 0
	global_load_lds_dwordx4 v0, s[62:63]
	v_mov_b32_e32 v0, v183
	s_add_i32 m0, s61, 0x2000
	s_nop 0
	global_load_lds_dwordx4 v0, s[62:63]
	s_waitcnt vmcnt(6)
	s_barrier
	s_setprio 1
	v_mfma_scale_f32_16x16x128_f8f6f4 v[104:107], v[196:203], v[16:23], 0, v195, v195 op_sel_hi:[0,0,0]
	v_mfma_scale_f32_16x16x128_f8f6f4 v[96:99], v[204:211], v[16:23], 0, v195, v195 op_sel_hi:[0,0,0]
	v_mfma_scale_f32_16x16x128_f8f6f4 v[88:91], v[196:203], v[24:31], 0, v195, v195 op_sel_hi:[0,0,0]
	v_mfma_scale_f32_16x16x128_f8f6f4 v[80:83], v[204:211], v[24:31], 0, v195, v195 op_sel_hi:[0,0,0]
	v_mfma_scale_f32_16x16x128_f8f6f4 v[72:75], v[196:203], v[32:39], 0, v195, v195 op_sel_hi:[0,0,0]
	v_mfma_scale_f32_16x16x128_f8f6f4 v[64:67], v[204:211], v[32:39], 0, v195, v195 op_sel_hi:[0,0,0]
	v_mfma_scale_f32_16x16x128_f8f6f4 v[56:59], v[196:203], v[40:47], 0, v195, v195 op_sel_hi:[0,0,0]
	v_mfma_scale_f32_16x16x128_f8f6f4 v[48:51], v[204:211], v[40:47], 0, v195, v195 op_sel_hi:[0,0,0]
	s_setprio 0
	s_add_i32 s61, 0, 0x18000
	v_add_u32_e32 v12, s61, v188
	s_barrier
	ds_read_b128 v[0:3], v12
	ds_read_b128 v[4:7], v12 offset:1024
	ds_read_b128 v[8:11], v12 offset:2048
	ds_read_b128 v[12:15], v12 offset:3072
	v_mov_b32_e32 v178, v186
	s_mov_b32 m0, s46
	ds_read_b128 v[16:19], v194 offset:32768
	ds_read_b128 v[20:23], v194 offset:33792
	ds_read_b128 v[24:27], v194 offset:34816
	ds_read_b128 v[28:31], v194 offset:35840
	ds_read_b128 v[32:35], v194 offset:36864
	ds_read_b128 v[36:39], v194 offset:37888
	ds_read_b128 v[40:43], v194 offset:38912
	ds_read_b128 v[44:47], v194 offset:39936
	s_nop 0
	global_load_lds_dwordx4 v178, s[40:41]
	v_mov_b32_e32 v178, v187
	s_mov_b32 m0, s47
	s_nop 0
	global_load_lds_dwordx4 v178, s[40:41]
	s_waitcnt lgkmcnt(8)
	s_barrier
	s_waitcnt lgkmcnt(0)
	s_setprio 1
	s_waitcnt lgkmcnt(0)
	v_mfma_scale_f32_16x16x128_f8f6f4 v[172:175], v[0:7], v[16:23], v[172:175], v195, v195 op_sel_hi:[0,0,0]
	v_mfma_scale_f32_16x16x128_f8f6f4 v[168:171], v[8:15], v[16:23], v[168:171], v195, v195 op_sel_hi:[0,0,0]
	v_mfma_scale_f32_16x16x128_f8f6f4 v[164:167], v[0:7], v[24:31], v[164:167], v195, v195 op_sel_hi:[0,0,0]
	v_mfma_scale_f32_16x16x128_f8f6f4 v[156:159], v[8:15], v[24:31], v[156:159], v195, v195 op_sel_hi:[0,0,0]
	v_mfma_scale_f32_16x16x128_f8f6f4 v[140:143], v[0:7], v[32:39], v[140:143], v195, v195 op_sel_hi:[0,0,0]
	v_mfma_scale_f32_16x16x128_f8f6f4 v[132:135], v[8:15], v[32:39], v[132:135], v195, v195 op_sel_hi:[0,0,0]
	v_mfma_scale_f32_16x16x128_f8f6f4 v[120:123], v[0:7], v[40:47], v[120:123], v195, v195 op_sel_hi:[0,0,0]
	v_mfma_scale_f32_16x16x128_f8f6f4 v[112:115], v[8:15], v[40:47], v[112:115], v195, v195 op_sel_hi:[0,0,0]
	s_setprio 0
	s_barrier
	s_add_i32 s62, 0, 0x1c000
	v_add_u32_e32 v178, s62, v188
	ds_read_b128 v[196:199], v178
	ds_read_b128 v[200:203], v178 offset:1024
	ds_read_b128 v[204:207], v178 offset:2048
	ds_read_b128 v[208:211], v178 offset:3072
	v_mov_b32_e32 v178, v181
	s_add_i32 s61, s61, s42
	v_lshl_add_u64 v[212:213], s[38:39], 0, v[178:179]
	v_lshl_add_u64 v[212:213], v[212:213], 0, s[12:13]
	s_mov_b32 m0, s61
	v_mov_b32_e32 v178, v183
	global_load_lds_dwordx4 v[212:213], off
	s_add_i32 m0, s61, 0x2000
	v_lshl_add_u64 v[212:213], s[38:39], 0, v[178:179]
	v_lshl_add_u64 v[212:213], v[212:213], 0, s[12:13]
	global_load_lds_dwordx4 v[212:213], off
	s_barrier
	s_waitcnt lgkmcnt(0)
	s_setprio 1
	s_waitcnt lgkmcnt(0)
	v_mfma_scale_f32_16x16x128_f8f6f4 v[160:163], v[196:203], v[16:23], v[160:163], v195, v195 op_sel_hi:[0,0,0]
	v_mfma_scale_f32_16x16x128_f8f6f4 v[152:155], v[204:211], v[16:23], v[152:155], v195, v195 op_sel_hi:[0,0,0]
	v_mfma_scale_f32_16x16x128_f8f6f4 v[148:151], v[196:203], v[24:31], v[148:151], v195, v195 op_sel_hi:[0,0,0]
	v_mfma_scale_f32_16x16x128_f8f6f4 v[144:147], v[204:211], v[24:31], v[144:147], v195, v195 op_sel_hi:[0,0,0]
	v_mfma_scale_f32_16x16x128_f8f6f4 v[136:139], v[196:203], v[32:39], v[136:139], v195, v195 op_sel_hi:[0,0,0]
	v_mfma_scale_f32_16x16x128_f8f6f4 v[128:131], v[204:211], v[32:39], v[128:131], v195, v195 op_sel_hi:[0,0,0]
	v_mfma_scale_f32_16x16x128_f8f6f4 v[124:127], v[196:203], v[40:47], v[124:127], v195, v195 op_sel_hi:[0,0,0]
	v_mfma_scale_f32_16x16x128_f8f6f4 v[116:119], v[204:211], v[40:47], v[116:119], v195, v195 op_sel_hi:[0,0,0]
	s_setprio 0
	v_mov_b32_e32 v178, v184
	s_barrier
	ds_read_b128 v[16:19], v194 offset:49152
	ds_read_b128 v[20:23], v194 offset:50176
	ds_read_b128 v[24:27], v194 offset:51200
	ds_read_b128 v[28:31], v194 offset:52224
	ds_read_b128 v[32:35], v194 offset:53248
	ds_read_b128 v[36:39], v194 offset:54272
	ds_read_b128 v[40:43], v194 offset:55296
	ds_read_b128 v[44:47], v194 offset:56320
	s_mov_b32 m0, s52
	v_lshl_add_u64 v[212:213], s[40:41], 0, v[178:179]
	v_lshl_add_u64 v[212:213], v[212:213], 0, s[12:13]
	v_mov_b32_e32 v178, v185
	global_load_lds_dwordx4 v[212:213], off
	s_mov_b32 m0, s53
	v_lshl_add_u64 v[212:213], s[40:41], 0, v[178:179]
	v_lshl_add_u64 v[212:213], v[212:213], 0, s[12:13]
	global_load_lds_dwordx4 v[212:213], off
	s_barrier
	s_waitcnt lgkmcnt(0)
	s_setprio 1
	s_waitcnt lgkmcnt(0)
	v_mfma_scale_f32_16x16x128_f8f6f4 v[108:111], v[0:7], v[16:23], v[108:111], v195, v195 op_sel_hi:[0,0,0]
	v_mfma_scale_f32_16x16x128_f8f6f4 v[100:103], v[8:15], v[16:23], v[100:103], v195, v195 op_sel_hi:[0,0,0]
	v_mfma_scale_f32_16x16x128_f8f6f4 v[92:95], v[0:7], v[24:31], v[92:95], v195, v195 op_sel_hi:[0,0,0]
	v_mfma_scale_f32_16x16x128_f8f6f4 v[84:87], v[8:15], v[24:31], v[84:87], v195, v195 op_sel_hi:[0,0,0]
	v_mfma_scale_f32_16x16x128_f8f6f4 v[76:79], v[0:7], v[32:39], v[76:79], v195, v195 op_sel_hi:[0,0,0]
	v_mfma_scale_f32_16x16x128_f8f6f4 v[68:71], v[8:15], v[32:39], v[68:71], v195, v195 op_sel_hi:[0,0,0]
	v_mfma_scale_f32_16x16x128_f8f6f4 v[60:63], v[0:7], v[40:47], v[60:63], v195, v195 op_sel_hi:[0,0,0]
	v_mfma_scale_f32_16x16x128_f8f6f4 v[52:55], v[8:15], v[40:47], v[52:55], v195, v195 op_sel_hi:[0,0,0]
	s_setprio 0
	s_barrier
	s_add_u32 s38, s38, 0x40080
	s_addc_u32 s39, s39, 0
	v_mov_b32_e32 v0, v181
	s_add_i32 s40, s62, s42
	s_mov_b32 m0, s40
	s_nop 0
	global_load_lds_dwordx4 v0, s[38:39]
	v_mov_b32_e32 v0, v183
	s_add_i32 m0, s40, 0x2000
	s_nop 0
	global_load_lds_dwordx4 v0, s[38:39]
	s_waitcnt vmcnt(6)
	s_barrier
	s_setprio 1
	v_mfma_scale_f32_16x16x128_f8f6f4 v[104:107], v[196:203], v[16:23], v[104:107], v195, v195 op_sel_hi:[0,0,0]
	v_mfma_scale_f32_16x16x128_f8f6f4 v[96:99], v[204:211], v[16:23], v[96:99], v195, v195 op_sel_hi:[0,0,0]
	v_mfma_scale_f32_16x16x128_f8f6f4 v[88:91], v[196:203], v[24:31], v[88:91], v195, v195 op_sel_hi:[0,0,0]
	v_mfma_scale_f32_16x16x128_f8f6f4 v[80:83], v[204:211], v[24:31], v[80:83], v195, v195 op_sel_hi:[0,0,0]
	v_mfma_scale_f32_16x16x128_f8f6f4 v[72:75], v[196:203], v[32:39], v[72:75], v195, v195 op_sel_hi:[0,0,0]
	v_mfma_scale_f32_16x16x128_f8f6f4 v[64:67], v[204:211], v[32:39], v[64:67], v195, v195 op_sel_hi:[0,0,0]
	v_mfma_scale_f32_16x16x128_f8f6f4 v[56:59], v[196:203], v[40:47], v[56:59], v195, v195 op_sel_hi:[0,0,0]
	v_mfma_scale_f32_16x16x128_f8f6f4 v[48:51], v[204:211], v[40:47], v[48:51], v195, v195 op_sel_hi:[0,0,0]
	s_setprio 0
	s_add_i32 s60, s60, 2
	s_add_u32 s36, s36, 0x100
	s_addc_u32 s37, s37, 0
	s_add_u32 s8, s8, 0x100
	s_addc_u32 s23, s23, 0
	s_cmp_gt_u32 s60, 13
	s_barrier
	s_cbranch_scc1 .LBB0_1936
	s_branch .LBB0_1945
